# HGRN forget-gate chain (both passes): the 16 raw gate-row LDS reads of a sub-chunk issued together at the section top into idle registers (one wait) instead of 16 exposed LDS round trips
# baseline (speedup 1.0000x reference)
.LBB0_362:
	v_add_u32_e32 v134, 0, v122
	ds_read2_b32 v[134:135], v134 offset1:68
	v_add_u32_e32 v136, 544, v122
	ds_read2_b32 v[136:137], v136 offset1:68
	v_add_u32_e32 v138, 1088, v122
	ds_read2_b32 v[138:139], v138 offset1:68
	v_add_u32_e32 v140, 1632, v122
	ds_read2_b32 v[140:141], v140 offset1:68
	v_add_u32_e32 v142, 2176, v122
	ds_read2_b32 v[142:143], v142 offset1:68
	v_add_u32_e32 v144, 2720, v122
	ds_read2_b32 v[144:145], v144 offset1:68
	v_add_u32_e32 v146, 3264, v122
	ds_read2_b32 v[146:147], v146 offset1:68
	v_add_u32_e32 v148, 3808, v122
	ds_read2_b32 v[148:149], v148 offset1:68
	v_add_u32_e32 v212, 4352, v122
	ds_read2_b32 v[212:213], v212 offset1:68
	v_add_u32_e32 v214, 4896, v122
	ds_read2_b32 v[214:215], v214 offset1:68
	v_add_u32_e32 v216, 5440, v122
	ds_read2_b32 v[216:217], v216 offset1:68
	v_add_u32_e32 v218, 5984, v122
	ds_read2_b32 v[218:219], v218 offset1:68
	v_add_u32_e32 v220, 6528, v122
	ds_read2_b32 v[220:221], v220 offset1:68
	v_add_u32_e32 v222, 7072, v122
	ds_read2_b32 v[222:223], v222 offset1:68
	v_add_u32_e32 v234, 7616, v122
	ds_read2_b32 v[234:235], v234 offset1:68
	v_add_u32_e32 v236, 8160, v122
	ds_read2_b32 v[236:237], v236 offset1:68
	s_waitcnt lgkmcnt(0)
	v_mov_b32_e32 v98, v134
	v_mov_b32_e32 v99, v135
	v_add_u32_e32 v102, 0x400, v122
	s_add_i32 s0, s0, 32
	s_cmpk_eq_i32 s0, 0x80
	v_mul_f32_e32 v98, 0xbfb8aa3b, v98
	v_exp_f32_e32 v98, v98
	v_mul_f32_e32 v99, 0xbfb8aa3b, v99
	v_exp_f32_e32 v99, v99
	v_add_f32_e32 v98, 1.0, v98
	v_rcp_f32_e32 v98, v98
	v_add_f32_e32 v99, 1.0, v99
	v_rcp_f32_e32 v99, v99
	v_fma_f32 v98, v131, v98, v117
	v_log_f32_e32 v100, v98
	v_fma_f32 v99, v131, v99, v117
	v_log_f32_e32 v101, v99
	v_sub_f32_e32 v98, 1.0, v98
	v_add_f32_e32 v100, 0, v100
	v_sub_f32_e32 v99, 1.0, v99
	v_add_f32_e32 v101, v100, v101
	ds_write2_b32 v122, v100, v101 offset1:68
	v_add_u32_e32 v100, 0x2000, v122
	ds_write2_b32 v100, v98, v99 offset0:128 offset1:196
	v_mov_b32_e32 v98, v136
	v_mov_b32_e32 v99, v137
	v_mul_f32_e32 v98, 0xbfb8aa3b, v98
	v_exp_f32_e32 v98, v98
	v_mul_f32_e32 v99, 0xbfb8aa3b, v99
	v_exp_f32_e32 v99, v99
	v_add_f32_e32 v98, 1.0, v98
	v_rcp_f32_e32 v98, v98
	v_add_f32_e32 v99, 1.0, v99
	v_rcp_f32_e32 v99, v99
	v_fma_f32 v98, v131, v98, v117
	v_log_f32_e32 v100, v98
	v_fma_f32 v99, v131, v99, v117
	v_sub_f32_e32 v98, 1.0, v98
	v_add_f32_e32 v100, v101, v100
	v_log_f32_e32 v101, v99
	v_sub_f32_e32 v99, 1.0, v99
	v_add_f32_e32 v101, v100, v101
	ds_write2_b32 v122, v100, v101 offset0:136 offset1:204
	v_add_u32_e32 v100, 0x2400, v122
	ds_write2_b32 v100, v98, v99 offset0:8 offset1:76
	v_mov_b32_e32 v98, v138
	v_mov_b32_e32 v99, v139
	v_mul_f32_e32 v98, 0xbfb8aa3b, v98
	v_exp_f32_e32 v98, v98
	v_mul_f32_e32 v99, 0xbfb8aa3b, v99
	v_exp_f32_e32 v99, v99
	v_add_f32_e32 v98, 1.0, v98
	v_rcp_f32_e32 v98, v98
	v_add_f32_e32 v99, 1.0, v99
	v_rcp_f32_e32 v99, v99
	v_fma_f32 v98, v131, v98, v117
	v_log_f32_e32 v103, v98
	v_fma_f32 v99, v131, v99, v117
	v_sub_f32_e32 v98, 1.0, v98
	v_add_f32_e32 v101, v101, v103
	v_log_f32_e32 v103, v99
	v_sub_f32_e32 v99, 1.0, v99
	ds_write2_b32 v100, v98, v99 offset0:144 offset1:212
	v_mov_b32_e32 v98, v140
	v_mov_b32_e32 v99, v141
	v_add_f32_e32 v103, v101, v103
	ds_write2_b32 v102, v101, v103 offset0:16 offset1:84
	v_mul_f32_e32 v98, 0xbfb8aa3b, v98
	v_exp_f32_e32 v98, v98
	v_mul_f32_e32 v99, 0xbfb8aa3b, v99
	v_exp_f32_e32 v99, v99
	v_add_f32_e32 v98, 1.0, v98
	v_rcp_f32_e32 v98, v98
	v_add_f32_e32 v99, 1.0, v99
	v_rcp_f32_e32 v99, v99
	v_fma_f32 v98, v131, v98, v117
	v_log_f32_e32 v100, v98
	v_fma_f32 v99, v131, v99, v117
	v_log_f32_e32 v101, v99
	v_sub_f32_e32 v98, 1.0, v98
	v_add_f32_e32 v100, v103, v100
	v_sub_f32_e32 v99, 1.0, v99
	v_add_f32_e32 v101, v100, v101
	ds_write2_b32 v102, v100, v101 offset0:152 offset1:220
	v_add_u32_e32 v100, 0x2800, v122
	v_add_u32_e32 v102, 0x800, v122
	ds_write2_b32 v100, v98, v99 offset0:24 offset1:92
	v_mov_b32_e32 v98, v142
	v_mov_b32_e32 v99, v143
	v_mul_f32_e32 v98, 0xbfb8aa3b, v98
	v_exp_f32_e32 v98, v98
	v_mul_f32_e32 v99, 0xbfb8aa3b, v99
	v_exp_f32_e32 v99, v99
	v_add_f32_e32 v98, 1.0, v98
	v_rcp_f32_e32 v98, v98
	v_add_f32_e32 v99, 1.0, v99
	v_rcp_f32_e32 v99, v99
	v_fma_f32 v98, v131, v98, v117
	v_log_f32_e32 v103, v98
	v_fma_f32 v99, v131, v99, v117
	v_sub_f32_e32 v98, 1.0, v98
	v_add_f32_e32 v101, v101, v103
	v_log_f32_e32 v103, v99
	v_sub_f32_e32 v99, 1.0, v99
	ds_write2_b32 v100, v98, v99 offset0:160 offset1:228
	v_mov_b32_e32 v98, v144
	v_mov_b32_e32 v99, v145
	v_add_f32_e32 v103, v101, v103
	ds_write2_b32 v102, v101, v103 offset0:32 offset1:100
	v_mul_f32_e32 v98, 0xbfb8aa3b, v98
	v_exp_f32_e32 v98, v98
	v_mul_f32_e32 v99, 0xbfb8aa3b, v99
	v_exp_f32_e32 v99, v99
	v_add_f32_e32 v98, 1.0, v98
	v_rcp_f32_e32 v98, v98
	v_add_f32_e32 v99, 1.0, v99
	v_rcp_f32_e32 v99, v99
	v_fma_f32 v98, v131, v98, v117
	v_log_f32_e32 v100, v98
	v_fma_f32 v99, v131, v99, v117
	v_log_f32_e32 v101, v99
	v_sub_f32_e32 v98, 1.0, v98
	v_add_f32_e32 v100, v103, v100
	v_sub_f32_e32 v99, 1.0, v99
	v_add_f32_e32 v101, v100, v101
	ds_write2_b32 v102, v100, v101 offset0:168 offset1:236
	v_add_u32_e32 v100, 0x2c00, v122
	v_add_u32_e32 v102, 0xc00, v122
	ds_write2_b32 v100, v98, v99 offset0:40 offset1:108
	v_mov_b32_e32 v98, v146
	v_mov_b32_e32 v99, v147
	v_mul_f32_e32 v98, 0xbfb8aa3b, v98
	v_exp_f32_e32 v98, v98
	v_mul_f32_e32 v99, 0xbfb8aa3b, v99
	v_exp_f32_e32 v99, v99
	v_add_f32_e32 v98, 1.0, v98
	v_rcp_f32_e32 v98, v98
	v_add_f32_e32 v99, 1.0, v99
	v_rcp_f32_e32 v99, v99
	v_fma_f32 v98, v131, v98, v117
	v_log_f32_e32 v103, v98
	v_fma_f32 v99, v131, v99, v117
	v_sub_f32_e32 v98, 1.0, v98
	v_add_f32_e32 v101, v101, v103
	v_log_f32_e32 v103, v99
	v_sub_f32_e32 v99, 1.0, v99
	ds_write2_b32 v100, v98, v99 offset0:176 offset1:244
	v_mov_b32_e32 v98, v148
	v_mov_b32_e32 v99, v149
	v_add_f32_e32 v103, v101, v103
	ds_write2_b32 v102, v101, v103 offset0:48 offset1:116
	v_mul_f32_e32 v98, 0xbfb8aa3b, v98
	v_exp_f32_e32 v98, v98
	v_mul_f32_e32 v99, 0xbfb8aa3b, v99
	v_exp_f32_e32 v99, v99
	v_add_f32_e32 v98, 1.0, v98
	v_rcp_f32_e32 v98, v98
	v_add_f32_e32 v99, 1.0, v99
	v_rcp_f32_e32 v99, v99
	v_fma_f32 v98, v131, v98, v117
	v_log_f32_e32 v100, v98
	v_fma_f32 v99, v131, v99, v117
	v_log_f32_e32 v101, v99
	v_sub_f32_e32 v98, 1.0, v98
	v_add_f32_e32 v100, v103, v100
	v_sub_f32_e32 v99, 1.0, v99
	v_add_f32_e32 v101, v100, v101
	ds_write2_b32 v102, v100, v101 offset0:184 offset1:252
	v_add_u32_e32 v100, 0x3000, v122
	ds_write2_b32 v100, v98, v99 offset0:56 offset1:124
	v_add_u32_e32 v100, 0x1000, v122
	v_mov_b32_e32 v98, v212
	v_mov_b32_e32 v99, v213
	v_mul_f32_e32 v98, 0xbfb8aa3b, v98
	v_exp_f32_e32 v98, v98
	v_mul_f32_e32 v99, 0xbfb8aa3b, v99
	v_exp_f32_e32 v99, v99
	v_add_f32_e32 v98, 1.0, v98
	v_rcp_f32_e32 v98, v98
	v_add_f32_e32 v99, 1.0, v99
	v_rcp_f32_e32 v99, v99
	v_fma_f32 v98, v131, v98, v117
	v_log_f32_e32 v102, v98
	v_fma_f32 v99, v131, v99, v117
	v_sub_f32_e32 v98, 1.0, v98
	v_add_f32_e32 v101, v101, v102
	v_log_f32_e32 v102, v99
	v_sub_f32_e32 v99, 1.0, v99
	v_add_f32_e32 v102, v101, v102
	ds_write2_b32 v100, v101, v102 offset0:64 offset1:132
	v_add_u32_e32 v100, 0x3200, v122
	ds_write2_b32 v100, v98, v99 offset0:64 offset1:132
	v_add_u32_e32 v100, 0x1200, v122
	v_mov_b32_e32 v98, v214
	v_mov_b32_e32 v99, v215
	v_mul_f32_e32 v98, 0xbfb8aa3b, v98
	v_exp_f32_e32 v98, v98
	v_mul_f32_e32 v99, 0xbfb8aa3b, v99
	v_exp_f32_e32 v99, v99
	v_add_f32_e32 v98, 1.0, v98
	v_rcp_f32_e32 v98, v98
	v_add_f32_e32 v99, 1.0, v99
	v_rcp_f32_e32 v99, v99
	v_fma_f32 v98, v131, v98, v117
	v_log_f32_e32 v101, v98
	v_fma_f32 v99, v131, v99, v117
	v_sub_f32_e32 v98, 1.0, v98
	v_add_f32_e32 v101, v102, v101
	v_log_f32_e32 v102, v99
	v_sub_f32_e32 v99, 1.0, v99
	v_add_f32_e32 v102, v101, v102
	ds_write2_b32 v100, v101, v102 offset0:72 offset1:140
	v_add_u32_e32 v100, 0x3400, v122
	ds_write2_b32 v100, v98, v99 offset0:72 offset1:140
	v_add_u32_e32 v100, 0x1400, v122
	v_mov_b32_e32 v98, v216
	v_mov_b32_e32 v99, v217
	v_mul_f32_e32 v98, 0xbfb8aa3b, v98
	v_exp_f32_e32 v98, v98
	v_mul_f32_e32 v99, 0xbfb8aa3b, v99
	v_exp_f32_e32 v99, v99
	v_add_f32_e32 v98, 1.0, v98
	v_rcp_f32_e32 v98, v98
	v_add_f32_e32 v99, 1.0, v99
	v_rcp_f32_e32 v99, v99
	v_fma_f32 v98, v131, v98, v117
	v_log_f32_e32 v101, v98
	v_fma_f32 v99, v131, v99, v117
	v_sub_f32_e32 v98, 1.0, v98
	v_add_f32_e32 v101, v102, v101
	v_log_f32_e32 v102, v99
	v_sub_f32_e32 v99, 1.0, v99
	v_add_f32_e32 v102, v101, v102
	ds_write2_b32 v100, v101, v102 offset0:80 offset1:148
	v_add_u32_e32 v100, 0x3600, v122
	ds_write2_b32 v100, v98, v99 offset0:80 offset1:148
	v_add_u32_e32 v100, 0x1600, v122
	v_mov_b32_e32 v98, v218
	v_mov_b32_e32 v99, v219
	v_mul_f32_e32 v98, 0xbfb8aa3b, v98
	v_exp_f32_e32 v98, v98
	v_mul_f32_e32 v99, 0xbfb8aa3b, v99
	v_exp_f32_e32 v99, v99
	v_add_f32_e32 v98, 1.0, v98
	v_rcp_f32_e32 v98, v98
	v_add_f32_e32 v99, 1.0, v99
	v_rcp_f32_e32 v99, v99
	v_fma_f32 v98, v131, v98, v117
	v_log_f32_e32 v101, v98
	v_fma_f32 v99, v131, v99, v117
	v_sub_f32_e32 v98, 1.0, v98
	v_add_f32_e32 v101, v102, v101
	v_log_f32_e32 v102, v99
	v_sub_f32_e32 v99, 1.0, v99
	v_add_f32_e32 v102, v101, v102
	ds_write2_b32 v100, v101, v102 offset0:88 offset1:156
	v_add_u32_e32 v100, 0x3800, v122
	ds_write2_b32 v100, v98, v99 offset0:88 offset1:156
	v_add_u32_e32 v100, 0x1800, v122
	v_mov_b32_e32 v98, v220
	v_mov_b32_e32 v99, v221
	v_mul_f32_e32 v98, 0xbfb8aa3b, v98
	v_exp_f32_e32 v98, v98
	v_mul_f32_e32 v99, 0xbfb8aa3b, v99
	v_exp_f32_e32 v99, v99
	v_add_f32_e32 v98, 1.0, v98
	v_rcp_f32_e32 v98, v98
	v_add_f32_e32 v99, 1.0, v99
	v_rcp_f32_e32 v99, v99
	v_fma_f32 v98, v131, v98, v117
	v_log_f32_e32 v101, v98
	v_fma_f32 v99, v131, v99, v117
	v_sub_f32_e32 v98, 1.0, v98
	v_add_f32_e32 v101, v102, v101
	v_log_f32_e32 v102, v99
	v_sub_f32_e32 v99, 1.0, v99
	v_add_f32_e32 v102, v101, v102
	ds_write2_b32 v100, v101, v102 offset0:96 offset1:164
	v_add_u32_e32 v100, 0x3a00, v122
	ds_write2_b32 v100, v98, v99 offset0:96 offset1:164
	v_add_u32_e32 v100, 0x1a00, v122
	v_mov_b32_e32 v98, v222
	v_mov_b32_e32 v99, v223
	v_mul_f32_e32 v98, 0xbfb8aa3b, v98
	v_exp_f32_e32 v98, v98
	v_mul_f32_e32 v99, 0xbfb8aa3b, v99
	v_exp_f32_e32 v99, v99
	v_add_f32_e32 v98, 1.0, v98
	v_rcp_f32_e32 v98, v98
	v_add_f32_e32 v99, 1.0, v99
	v_rcp_f32_e32 v99, v99
	v_fma_f32 v98, v131, v98, v117
	v_log_f32_e32 v101, v98
	v_fma_f32 v99, v131, v99, v117
	v_sub_f32_e32 v98, 1.0, v98
	v_add_f32_e32 v101, v102, v101
	v_log_f32_e32 v102, v99
	v_sub_f32_e32 v99, 1.0, v99
	v_add_f32_e32 v102, v101, v102
	ds_write2_b32 v100, v101, v102 offset0:104 offset1:172
	v_add_u32_e32 v100, 0x3c00, v122
	ds_write2_b32 v100, v98, v99 offset0:104 offset1:172
	v_add_u32_e32 v100, 0x1c00, v122
	v_mov_b32_e32 v98, v234
	v_mov_b32_e32 v99, v235
	v_mul_f32_e32 v98, 0xbfb8aa3b, v98
	v_exp_f32_e32 v98, v98
	v_mul_f32_e32 v99, 0xbfb8aa3b, v99
	v_exp_f32_e32 v99, v99
	v_add_f32_e32 v98, 1.0, v98
	v_rcp_f32_e32 v98, v98
	v_add_f32_e32 v99, 1.0, v99
	v_rcp_f32_e32 v99, v99
	v_fma_f32 v98, v131, v98, v117
	v_log_f32_e32 v101, v98
	v_fma_f32 v99, v131, v99, v117
	v_sub_f32_e32 v98, 1.0, v98
	v_add_f32_e32 v101, v102, v101
	v_log_f32_e32 v102, v99
	v_sub_f32_e32 v99, 1.0, v99
	v_add_f32_e32 v102, v101, v102
	ds_write2_b32 v100, v101, v102 offset0:112 offset1:180
	v_add_u32_e32 v100, 0x3e00, v122
	ds_write2_b32 v100, v98, v99 offset0:112 offset1:180
	v_add_u32_e32 v100, 0x1e00, v122
	v_mov_b32_e32 v98, v236
	v_mov_b32_e32 v99, v237
	v_mul_f32_e32 v98, 0xbfb8aa3b, v98
	v_exp_f32_e32 v98, v98
	v_mul_f32_e32 v99, 0xbfb8aa3b, v99
	v_exp_f32_e32 v99, v99
	v_add_f32_e32 v98, 1.0, v98
	v_rcp_f32_e32 v98, v98
	v_add_f32_e32 v99, 1.0, v99
	v_rcp_f32_e32 v99, v99
	v_fma_f32 v98, v131, v98, v117
	v_log_f32_e32 v101, v98
	v_fma_f32 v99, v131, v99, v117
	v_sub_f32_e32 v98, 1.0, v98
	v_add_f32_e32 v101, v102, v101
	v_log_f32_e32 v102, v99
	v_sub_f32_e32 v99, 1.0, v99
	v_add_f32_e32 v132, v101, v102
	ds_write2_b32 v100, v101, v132 offset0:120 offset1:188
	v_add_u32_e32 v100, 0x4000, v122
	ds_write2_b32 v100, v98, v99 offset0:120 offset1:188
	v_exp_f32_e32 v98, v132
	v_add_f32_e32 v1, v1, v132
	ds_write2st64_b32 v122, v98, v132 offset0:122 offset1:123
	ds_read_b128 v[106:109], v129 offset:26112
	ds_read_b128 v[98:101], v129 offset:26144
	ds_read_b128 v[110:113], v129 offset:28672
	ds_read_b128 v[102:105], v129 offset:28704
	ds_read_b128 v[134:137], v123 offset:31232
	ds_read_b128 v[138:141], v123 offset:31264
	ds_read_b128 v[142:145], v123 offset:31296
	ds_read_b128 v[146:149], v123 offset:31328
	s_waitcnt lgkmcnt(3)
	v_pk_mul_f32 v[34:35], v[34:35], v[134:135]
	v_pk_mul_f32 v[50:51], v[50:51], v[134:135]
	ds_read_b32 v133, v124 offset:31488
	ds_read2st64_b32 v[134:135], v125 offset1:34
	s_waitcnt lgkmcnt(4)
	v_pk_mul_f32 v[38:39], v[38:39], v[138:139]
	v_pk_mul_f32 v[54:55], v[54:55], v[138:139]
	v_pk_mul_f32 v[36:37], v[36:37], v[136:137]
	v_pk_mul_f32 v[52:53], v[52:53], v[136:137]
	s_waitcnt lgkmcnt(0)
	v_sub_f32_e32 v134, v133, v134
	v_exp_f32_e32 v134, v134
	v_pk_mul_f32 v[40:41], v[40:41], v[140:141]
	v_pk_mul_f32 v[56:57], v[56:57], v[140:141]
	v_pk_mul_f32 v[42:43], v[42:43], v[142:143]
	v_mul_f32_e32 v138, v135, v134
	v_add_u32_e32 v134, 0x2200, v127
	ds_read2_b32 v[134:135], v134 offset0:68 offset1:136
	ds_read2_b32 v[136:137], v127 offset0:68 offset1:136
	v_pk_mul_f32 v[58:59], v[58:59], v[142:143]
	v_pk_mul_f32 v[48:49], v[48:49], v[148:149]
	v_pk_mul_f32 v[44:45], v[44:45], v[144:145]
	v_pk_mul_f32 v[46:47], v[46:47], v[146:147]
	s_waitcnt lgkmcnt(0)
	v_sub_f32_e32 v136, v133, v136
	v_exp_f32_e32 v136, v136
	v_pk_mul_f32 v[64:65], v[64:65], v[148:149]
	v_pk_mul_f32 v[60:61], v[60:61], v[144:145]
	v_pk_mul_f32 v[62:63], v[62:63], v[146:147]
	v_mul_f32_e32 v139, v134, v136
	v_sub_f32_e32 v134, v133, v137
	v_add_u32_e32 v136, 0x200, v127
	v_exp_f32_e32 v134, v134
	ds_read2_b32 v[136:137], v136 offset0:76 offset1:144
	v_mul_f32_e32 v140, v135, v134
	v_add_u32_e32 v134, 0x2400, v127
	ds_read2_b32 v[134:135], v134 offset0:76 offset1:144
	s_waitcnt lgkmcnt(1)
	v_sub_f32_e32 v136, v133, v136
	v_exp_f32_e32 v136, v136
	s_waitcnt lgkmcnt(0)
	v_mul_f32_e32 v141, v134, v136
	v_sub_f32_e32 v134, v133, v137
	v_add_u32_e32 v136, 0x400, v127
	v_exp_f32_e32 v134, v134
	ds_read2_b32 v[136:137], v136 offset0:84 offset1:152
	v_mul_f32_e32 v142, v135, v134
	v_add_u32_e32 v134, 0x2600, v127
	ds_read2_b32 v[134:135], v134 offset0:84 offset1:152
	s_waitcnt lgkmcnt(1)
	v_sub_f32_e32 v136, v133, v136
	v_exp_f32_e32 v136, v136
	s_waitcnt lgkmcnt(0)
	v_mul_f32_e32 v136, v134, v136
	v_sub_f32_e32 v134, v133, v137
	v_exp_f32_e32 v134, v134
	s_nop 0
	v_mul_f32_e32 v137, v135, v134
	ds_read_b32 v134, v127 offset:10608
	ds_read_b32 v135, v127 offset:1904
	s_waitcnt lgkmcnt(0)
	v_sub_f32_e32 v135, v133, v135
	v_exp_f32_e32 v135, v135
	s_nop 0
	v_mul_f32_e32 v143, v134, v135
	v_cvt_pk_bf16_f32 v134, v138, v139
	s_nop 1
	v_cvt_pk_bf16_f32 v135, v140, v141
	s_nop 1
	v_cvt_pk_bf16_f32 v136, v142, v136
	s_nop 1
	v_cvt_pk_bf16_f32 v137, v137, v143
	s_nop 1
	s_nop 0
	v_mfma_f32_32x32x16_bf16 v[34:49], v[134:137], v[106:109], v[34:49]
	v_mfma_f32_32x32x16_bf16 v[50:65], v[134:137], v[110:113], v[50:65]
	v_add_u32_e32 v136, 0x1000, v127
	ds_read2_b32 v[136:137], v136 offset0:64 offset1:132
	v_add_u32_e32 v134, 0x3200, v127
	ds_read2_b32 v[134:135], v134 offset0:64 offset1:132
	s_waitcnt lgkmcnt(1)
	v_sub_f32_e32 v136, v133, v136
	v_exp_f32_e32 v136, v136
	s_waitcnt lgkmcnt(0)
	v_mul_f32_e32 v138, v134, v136
	v_sub_f32_e32 v134, v133, v137
	v_add_u32_e32 v136, 0x1200, v127
	v_exp_f32_e32 v134, v134
	ds_read2_b32 v[136:137], v136 offset0:72 offset1:140
	v_mul_f32_e32 v139, v135, v134
	v_add_u32_e32 v134, 0x3400, v127
	ds_read2_b32 v[134:135], v134 offset0:72 offset1:140
	s_waitcnt lgkmcnt(1)
	v_sub_f32_e32 v136, v133, v136
	v_exp_f32_e32 v136, v136
	s_waitcnt lgkmcnt(0)
	v_mul_f32_e32 v140, v134, v136
	v_sub_f32_e32 v134, v133, v137
	v_add_u32_e32 v136, 0x1400, v127
	v_exp_f32_e32 v134, v134
	ds_read2_b32 v[136:137], v136 offset0:80 offset1:148
	v_mul_f32_e32 v141, v135, v134
	v_add_u32_e32 v134, 0x3600, v127
	ds_read2_b32 v[134:135], v134 offset0:80 offset1:148
	s_waitcnt lgkmcnt(1)
	v_sub_f32_e32 v136, v133, v136
	v_exp_f32_e32 v136, v136
	s_waitcnt lgkmcnt(0)
	v_mul_f32_e32 v142, v134, v136
	v_sub_f32_e32 v134, v133, v137
	v_add_u32_e32 v136, 0x1600, v127
	v_exp_f32_e32 v134, v134
	ds_read2_b32 v[136:137], v136 offset0:88 offset1:156
	v_mul_f32_e32 v143, v135, v134
	v_add_u32_e32 v134, 0x3800, v127
	ds_read2_b32 v[134:135], v134 offset0:88 offset1:156
	s_waitcnt lgkmcnt(1)
	v_sub_f32_e32 v136, v133, v136
	v_sub_f32_e32 v133, v133, v137
	v_exp_f32_e32 v136, v136
	v_exp_f32_e32 v133, v133
	s_waitcnt lgkmcnt(0)
	v_mul_f32_e32 v144, v134, v136
	v_mul_f32_e32 v133, v135, v133
	v_cvt_pk_bf16_f32 v134, v138, v139
	s_nop 1
	v_cvt_pk_bf16_f32 v135, v140, v141
	s_nop 1
	v_cvt_pk_bf16_f32 v136, v142, v143
	s_nop 1
	v_cvt_pk_bf16_f32 v137, v144, v133
	s_nop 1
	s_nop 0
	v_mfma_f32_32x32x16_bf16 v[34:49], v[134:137], v[98:101], v[34:49]
	v_mfma_f32_32x32x16_bf16 v[50:65], v[134:137], v[102:105], v[50:65]
	ds_read_b128 v[134:137], v123 offset:31360
	ds_read_b128 v[138:141], v123 offset:31392
	ds_read_b128 v[142:145], v123 offset:31424
	ds_read_b128 v[146:149], v123 offset:31456
	ds_read_b32 v133, v124 offset:31616
	s_waitcnt lgkmcnt(4)
	v_pk_mul_f32 v[18:19], v[18:19], v[134:135]
	v_pk_mul_f32 v[2:3], v[2:3], v[134:135]
	v_add_u32_e32 v134, 0x80, v127
	ds_read2st64_b32 v[134:135], v134 offset1:34
	s_waitcnt lgkmcnt(4)
	v_pk_mul_f32 v[22:23], v[22:23], v[138:139]
	v_pk_mul_f32 v[6:7], v[6:7], v[138:139]
	v_pk_mul_f32 v[20:21], v[20:21], v[136:137]
	v_pk_mul_f32 v[4:5], v[4:5], v[136:137]
	s_waitcnt lgkmcnt(0)
	v_sub_f32_e32 v134, v133, v134
	v_exp_f32_e32 v134, v134
	v_pk_mul_f32 v[24:25], v[24:25], v[140:141]
	v_pk_mul_f32 v[8:9], v[8:9], v[140:141]
	v_pk_mul_f32 v[26:27], v[26:27], v[142:143]
	v_mul_f32_e32 v138, v135, v134
	v_add_u32_e32 v134, 0x2200, v130
	ds_read2_b32 v[134:135], v134 offset0:68 offset1:136
	ds_read2_b32 v[136:137], v130 offset0:68 offset1:136
	v_pk_mul_f32 v[10:11], v[10:11], v[142:143]
	v_pk_mul_f32 v[32:33], v[32:33], v[148:149]
	v_pk_mul_f32 v[28:29], v[28:29], v[144:145]
	v_pk_mul_f32 v[30:31], v[30:31], v[146:147]
	s_waitcnt lgkmcnt(0)
	v_sub_f32_e32 v136, v133, v136
	v_exp_f32_e32 v136, v136
	v_pk_mul_f32 v[16:17], v[16:17], v[148:149]
	v_pk_mul_f32 v[12:13], v[12:13], v[144:145]
	v_pk_mul_f32 v[14:15], v[14:15], v[146:147]
	v_mul_f32_e32 v139, v134, v136
	v_sub_f32_e32 v134, v133, v137
	v_add_u32_e32 v136, 0x200, v130
	v_exp_f32_e32 v134, v134
	ds_read2_b32 v[136:137], v136 offset0:76 offset1:144
	v_mul_f32_e32 v140, v135, v134
	v_add_u32_e32 v134, 0x2400, v130
	ds_read2_b32 v[134:135], v134 offset0:76 offset1:144
	s_waitcnt lgkmcnt(1)
	v_sub_f32_e32 v136, v133, v136
	v_exp_f32_e32 v136, v136
	s_waitcnt lgkmcnt(0)
	v_mul_f32_e32 v141, v134, v136
	v_sub_f32_e32 v134, v133, v137
	v_add_u32_e32 v136, 0x400, v130
	v_exp_f32_e32 v134, v134
	ds_read2_b32 v[136:137], v136 offset0:84 offset1:152
	v_mul_f32_e32 v142, v135, v134
	v_add_u32_e32 v134, 0x2600, v130
	ds_read2_b32 v[134:135], v134 offset0:84 offset1:152
	s_waitcnt lgkmcnt(1)
	v_sub_f32_e32 v136, v133, v136
	v_exp_f32_e32 v136, v136
	s_waitcnt lgkmcnt(0)
	v_mul_f32_e32 v136, v134, v136
	v_sub_f32_e32 v134, v133, v137
	v_exp_f32_e32 v134, v134
	s_nop 0
	v_mul_f32_e32 v137, v135, v134
	ds_read_b32 v134, v130 offset:10608
	ds_read_b32 v135, v130 offset:1904
	s_waitcnt lgkmcnt(0)
	v_sub_f32_e32 v135, v133, v135
	v_exp_f32_e32 v135, v135
	s_nop 0
	v_mul_f32_e32 v143, v134, v135
	v_cvt_pk_bf16_f32 v134, v138, v139
	s_nop 1
	v_cvt_pk_bf16_f32 v135, v140, v141
	s_nop 1
	v_cvt_pk_bf16_f32 v136, v142, v136
	s_nop 1
	v_cvt_pk_bf16_f32 v137, v137, v143
	s_nop 1
	s_nop 0
	v_mfma_f32_32x32x16_bf16 v[18:33], v[134:137], v[106:109], v[18:33]
	v_add_u32_e32 v108, 0x1000, v130
	ds_read2_b32 v[108:109], v108 offset0:64 offset1:132
	v_add_u32_e32 v106, 0x3200, v130
	ds_read2_b32 v[106:107], v106 offset0:64 offset1:132
	s_waitcnt lgkmcnt(1)
	v_sub_f32_e32 v108, v133, v108
	v_exp_f32_e32 v108, v108
	v_mfma_f32_32x32x16_bf16 v[2:17], v[134:137], v[110:113], v[2:17]
	s_waitcnt lgkmcnt(0)
	v_mul_f32_e32 v110, v106, v108
	v_sub_f32_e32 v106, v133, v109
	v_add_u32_e32 v108, 0x1200, v130
	v_exp_f32_e32 v106, v106
	ds_read2_b32 v[108:109], v108 offset0:72 offset1:140
	v_mul_f32_e32 v111, v107, v106
	v_add_u32_e32 v106, 0x3400, v130
	ds_read2_b32 v[106:107], v106 offset0:72 offset1:140
	s_waitcnt lgkmcnt(1)
	v_sub_f32_e32 v108, v133, v108
	v_exp_f32_e32 v108, v108
	s_waitcnt lgkmcnt(0)
	v_mul_f32_e32 v112, v106, v108
	v_sub_f32_e32 v106, v133, v109
	v_add_u32_e32 v108, 0x1400, v130
	v_exp_f32_e32 v106, v106
	ds_read2_b32 v[108:109], v108 offset0:80 offset1:148
	v_mul_f32_e32 v113, v107, v106
	v_add_u32_e32 v106, 0x3600, v130
	ds_read2_b32 v[106:107], v106 offset0:80 offset1:148
	s_waitcnt lgkmcnt(1)
	v_sub_f32_e32 v108, v133, v108
	v_exp_f32_e32 v108, v108
	s_waitcnt lgkmcnt(0)
	v_mul_f32_e32 v134, v106, v108
	v_sub_f32_e32 v106, v133, v109
	v_add_u32_e32 v108, 0x1600, v130
	v_exp_f32_e32 v106, v106
	ds_read2_b32 v[108:109], v108 offset0:88 offset1:156
	v_mul_f32_e32 v135, v107, v106
	v_add_u32_e32 v106, 0x3800, v130
	ds_read2_b32 v[106:107], v106 offset0:88 offset1:156
	s_waitcnt lgkmcnt(1)
	v_sub_f32_e32 v108, v133, v108
	v_exp_f32_e32 v108, v108
	s_waitcnt lgkmcnt(0)
	v_mul_f32_e32 v136, v106, v108
	v_sub_f32_e32 v106, v133, v109
	v_exp_f32_e32 v106, v106
	s_nop 0
	v_mul_f32_e32 v109, v107, v106
	v_cvt_pk_bf16_f32 v106, v110, v111
	s_nop 1
	v_cvt_pk_bf16_f32 v107, v112, v113
	s_nop 1
	v_cvt_pk_bf16_f32 v108, v134, v135
	s_nop 1
	v_cvt_pk_bf16_f32 v109, v136, v109
	s_nop 1
	s_nop 1
	v_mfma_f32_32x32x16_bf16 v[18:33], v[106:109], v[98:101], v[18:33]
	v_mfma_f32_32x32x16_bf16 v[2:17], v[106:109], v[102:105], v[2:17]
	s_cbranch_scc1 .LBB0_358

.LBB0_1000:
	v_add_u32_e32 v148, 0, v179
	ds_read2_b32 v[148:149], v148 offset1:68
	v_add_u32_e32 v150, 544, v179
	ds_read2_b32 v[150:151], v150 offset1:68
	v_add_u32_e32 v152, 1088, v179
	ds_read2_b32 v[152:153], v152 offset1:68
	v_add_u32_e32 v154, 1632, v179
	ds_read2_b32 v[154:155], v154 offset1:68
	v_add_u32_e32 v156, 2176, v179
	ds_read2_b32 v[156:157], v156 offset1:68
	v_add_u32_e32 v158, 2720, v179
	ds_read2_b32 v[158:159], v158 offset1:68
	v_add_u32_e32 v160, 3264, v179
	ds_read2_b32 v[160:161], v160 offset1:68
	v_add_u32_e32 v162, 3808, v179
	ds_read2_b32 v[162:163], v162 offset1:68
	v_add_u32_e32 v164, 4352, v179
	ds_read2_b32 v[164:165], v164 offset1:68
	v_add_u32_e32 v166, 4896, v179
	ds_read2_b32 v[166:167], v166 offset1:68
	v_add_u32_e32 v216, 5440, v179
	ds_read2_b32 v[216:217], v216 offset1:68
	v_add_u32_e32 v218, 5984, v179
	ds_read2_b32 v[218:219], v218 offset1:68
	v_add_u32_e32 v220, 6528, v179
	ds_read2_b32 v[220:221], v220 offset1:68
	v_add_u32_e32 v222, 7072, v179
	ds_read2_b32 v[222:223], v222 offset1:68
	v_add_u32_e32 v234, 7616, v179
	ds_read2_b32 v[234:235], v234 offset1:68
	v_add_u32_e32 v236, 8160, v179
	ds_read2_b32 v[236:237], v236 offset1:68
	s_waitcnt lgkmcnt(0)
	v_mov_b32_e32 v66, v148
	v_mov_b32_e32 v67, v149
	v_add_u32_e32 v70, 0x2000, v179
	v_add_u32_e32 v77, 0x1000, v179
	v_add_u32_e32 v78, 0x1600, v179
	v_mov_b32_e32 v74, 0
	v_mul_f32_e32 v66, 0xbfb8aa3b, v66
	v_mul_f32_e32 v67, 0xbfb8aa3b, v67
	v_exp_f32_e32 v68, v66
	v_exp_f32_e32 v69, v67
	v_mov_b32_e32 v66, v150
	v_mov_b32_e32 v67, v151
	s_mov_b32 s22, 0
	v_add_f32_e32 v68, 1.0, v68
	v_add_f32_e32 v69, 1.0, v69
	v_rcp_f32_e32 v68, v68
	v_rcp_f32_e32 v69, v69
	v_mul_f32_e32 v66, 0xbfb8aa3b, v66
	v_exp_f32_e32 v66, v66
	v_fma_f32 v68, v178, v68, v1
	v_fma_f32 v69, v178, v69, v1
	v_log_f32_e32 v71, v68
	v_log_f32_e32 v72, v69
	v_add_f32_e32 v66, 1.0, v66
	v_mul_f32_e32 v67, 0xbfb8aa3b, v67
	v_rcp_f32_e32 v66, v66
	v_exp_f32_e32 v67, v67
	v_add_f32_e32 v71, 0, v71
	v_sub_f32_e32 v68, 1.0, v68
	v_sub_f32_e32 v69, 1.0, v69
	v_add_f32_e32 v72, v71, v72
	ds_write2_b32 v179, v71, v72 offset1:68
	ds_write2_b32 v70, v68, v69 offset0:128 offset1:196
	v_fma_f32 v68, v178, v66, v1
	v_add_f32_e32 v66, 1.0, v67
	v_add_u32_e32 v71, 0x400, v179
	v_rcp_f32_e32 v70, v66
	v_mov_b32_e32 v66, v152
	v_mov_b32_e32 v67, v153
	v_log_f32_e32 v69, v68
	v_sub_f32_e32 v68, 1.0, v68
	v_fma_f32 v70, v178, v70, v1
	v_mov_b32_e32 v79, v74
	v_mul_f32_e32 v66, 0xbfb8aa3b, v66
	v_exp_f32_e32 v66, v66
	v_mul_f32_e32 v67, 0xbfb8aa3b, v67
	v_exp_f32_e32 v67, v67
	v_add_f32_e32 v69, v72, v69
	v_add_f32_e32 v66, 1.0, v66
	v_rcp_f32_e32 v66, v66
	v_log_f32_e32 v72, v70
	v_mov_b32_e32 v80, v74
	v_mov_b32_e32 v81, v74
	v_fma_f32 v73, v178, v66, v1
	v_add_f32_e32 v66, 1.0, v67
	v_rcp_f32_e32 v76, v66
	v_mov_b32_e32 v66, v154
	v_mov_b32_e32 v67, v155
	v_log_f32_e32 v75, v73
	v_add_f32_e32 v72, v69, v72
	ds_write2_b32 v179, v69, v72 offset0:136 offset1:204
	v_sub_f32_e32 v69, 1.0, v70
	v_mul_f32_e32 v66, 0xbfb8aa3b, v66
	v_exp_f32_e32 v66, v66
	v_add_u32_e32 v70, 0x2400, v179
	ds_write2_b32 v70, v68, v69 offset0:8 offset1:76
	v_fma_f32 v69, v178, v76, v1
	v_add_f32_e32 v68, v72, v75
	v_log_f32_e32 v72, v69
	v_add_f32_e32 v66, 1.0, v66
	v_mul_f32_e32 v67, 0xbfb8aa3b, v67
	v_rcp_f32_e32 v66, v66
	v_exp_f32_e32 v67, v67
	v_add_f32_e32 v72, v68, v72
	v_sub_f32_e32 v73, 1.0, v73
	ds_write2_b32 v71, v68, v72 offset0:16 offset1:84
	v_sub_f32_e32 v68, 1.0, v69
	ds_write2_b32 v70, v73, v68 offset0:144 offset1:212
	v_fma_f32 v68, v178, v66, v1
	v_add_f32_e32 v66, 1.0, v67
	v_add_u32_e32 v73, 0x800, v179
	v_rcp_f32_e32 v70, v66
	v_mov_b32_e32 v66, v156
	v_mov_b32_e32 v67, v157
	v_log_f32_e32 v69, v68
	v_sub_f32_e32 v68, 1.0, v68
	v_fma_f32 v70, v178, v70, v1
	v_mul_f32_e32 v66, 0xbfb8aa3b, v66
	v_exp_f32_e32 v66, v66
	v_add_f32_e32 v69, v72, v69
	v_log_f32_e32 v72, v70
	v_mul_f32_e32 v67, 0xbfb8aa3b, v67
	v_add_f32_e32 v66, 1.0, v66
	v_rcp_f32_e32 v66, v66
	v_exp_f32_e32 v67, v67
	v_add_f32_e32 v72, v69, v72
	ds_write2_b32 v71, v69, v72 offset0:152 offset1:220
	v_fma_f32 v71, v178, v66, v1
	v_add_f32_e32 v66, 1.0, v67
	v_rcp_f32_e32 v76, v66
	v_mov_b32_e32 v66, v158
	v_mov_b32_e32 v67, v159
	v_log_f32_e32 v75, v71
	v_sub_f32_e32 v69, 1.0, v70
	v_add_u32_e32 v70, 0x2800, v179
	ds_write2_b32 v70, v68, v69 offset0:24 offset1:92
	v_mul_f32_e32 v66, 0xbfb8aa3b, v66
	v_exp_f32_e32 v66, v66
	v_fma_f32 v69, v178, v76, v1
	v_add_f32_e32 v68, v72, v75
	v_log_f32_e32 v72, v69
	v_add_f32_e32 v66, 1.0, v66
	v_mul_f32_e32 v67, 0xbfb8aa3b, v67
	v_rcp_f32_e32 v66, v66
	v_exp_f32_e32 v67, v67
	v_add_f32_e32 v72, v68, v72
	v_sub_f32_e32 v71, 1.0, v71
	ds_write2_b32 v73, v68, v72 offset0:32 offset1:100
	v_sub_f32_e32 v68, 1.0, v69
	ds_write2_b32 v70, v71, v68 offset0:160 offset1:228
	v_fma_f32 v68, v178, v66, v1
	v_add_f32_e32 v66, 1.0, v67
	v_add_u32_e32 v71, 0xc00, v179
	v_rcp_f32_e32 v70, v66
	v_mov_b32_e32 v66, v160
	v_mov_b32_e32 v67, v161
	v_log_f32_e32 v69, v68
	v_sub_f32_e32 v68, 1.0, v68
	v_fma_f32 v70, v178, v70, v1
	v_mul_f32_e32 v66, 0xbfb8aa3b, v66
	v_exp_f32_e32 v66, v66
	v_add_f32_e32 v69, v72, v69
	v_log_f32_e32 v72, v70
	v_mul_f32_e32 v67, 0xbfb8aa3b, v67
	v_add_f32_e32 v66, 1.0, v66
	v_rcp_f32_e32 v66, v66
	v_exp_f32_e32 v67, v67
	v_add_f32_e32 v72, v69, v72
	ds_write2_b32 v73, v69, v72 offset0:168 offset1:236
	v_fma_f32 v73, v178, v66, v1
	v_add_f32_e32 v66, 1.0, v67
	v_rcp_f32_e32 v76, v66
	v_mov_b32_e32 v66, v162
	v_mov_b32_e32 v67, v163
	v_log_f32_e32 v75, v73
	v_sub_f32_e32 v69, 1.0, v70
	v_add_u32_e32 v70, 0x2c00, v179
	ds_write2_b32 v70, v68, v69 offset0:40 offset1:108
	v_mul_f32_e32 v66, 0xbfb8aa3b, v66
	v_exp_f32_e32 v66, v66
	v_fma_f32 v69, v178, v76, v1
	v_add_f32_e32 v68, v72, v75
	v_log_f32_e32 v72, v69
	v_add_f32_e32 v66, 1.0, v66
	v_mul_f32_e32 v67, 0xbfb8aa3b, v67
	v_rcp_f32_e32 v66, v66
	v_exp_f32_e32 v67, v67
	v_add_f32_e32 v72, v68, v72
	ds_write2_b32 v71, v68, v72 offset0:48 offset1:116
	v_sub_f32_e32 v68, 1.0, v69
	v_fma_f32 v69, v178, v66, v1
	v_add_f32_e32 v66, 1.0, v67
	v_rcp_f32_e32 v76, v66
	v_mov_b32_e32 v66, v164
	v_mov_b32_e32 v67, v165
	v_log_f32_e32 v75, v69
	v_sub_f32_e32 v73, 1.0, v73
	ds_write2_b32 v70, v73, v68 offset0:176 offset1:244
	v_fma_f32 v70, v178, v76, v1
	v_mul_f32_e32 v66, 0xbfb8aa3b, v66
	v_exp_f32_e32 v66, v66
	v_add_f32_e32 v68, v72, v75
	v_log_f32_e32 v72, v70
	v_mul_f32_e32 v67, 0xbfb8aa3b, v67
	v_add_f32_e32 v66, 1.0, v66
	v_rcp_f32_e32 v66, v66
	v_exp_f32_e32 v67, v67
	v_add_f32_e32 v72, v68, v72
	ds_write2_b32 v71, v68, v72 offset0:184 offset1:252
	v_sub_f32_e32 v68, 1.0, v70
	v_fma_f32 v70, v178, v66, v1
	v_log_f32_e32 v66, v70
	v_add_f32_e32 v67, 1.0, v67
	v_rcp_f32_e32 v67, v67
	v_sub_f32_e32 v69, 1.0, v69
	v_add_u32_e32 v71, 0x3000, v179
	ds_write2_b32 v71, v69, v68 offset0:56 offset1:124
	v_add_f32_e32 v68, v72, v66
	v_add_u32_e32 v72, 0x1200, v179
	v_fma_f32 v69, v178, v67, v1
	v_mov_b32_e32 v66, v166
	v_mov_b32_e32 v67, v167
	v_log_f32_e32 v71, v69
	v_sub_f32_e32 v70, 1.0, v70
	v_add_u32_e32 v75, 0x1400, v179
	v_mul_f32_e32 v66, 0xbfb8aa3b, v66
	v_mul_f32_e32 v67, 0xbfb8aa3b, v67
	v_exp_f32_e32 v66, v66
	v_exp_f32_e32 v67, v67
	v_add_f32_e32 v71, v68, v71
	ds_write2_b32 v77, v68, v71 offset0:64 offset1:132
	v_add_f32_e32 v66, 1.0, v66
	v_add_f32_e32 v67, 1.0, v67
	v_rcp_f32_e32 v66, v66
	v_rcp_f32_e32 v67, v67
	v_sub_f32_e32 v68, 1.0, v69
	v_add_u32_e32 v69, 0x3200, v179
	ds_write2_b32 v69, v70, v68 offset0:64 offset1:132
	v_fma_f32 v68, v178, v66, v1
	v_fma_f32 v70, v178, v67, v1
	v_mov_b32_e32 v66, v216
	v_mov_b32_e32 v67, v217
	v_log_f32_e32 v69, v68
	v_log_f32_e32 v73, v70
	v_sub_f32_e32 v68, 1.0, v68
	v_mul_f32_e32 v66, 0xbfb8aa3b, v66
	v_mul_f32_e32 v67, 0xbfb8aa3b, v67
	v_exp_f32_e32 v66, v66
	v_exp_f32_e32 v67, v67
	v_add_f32_e32 v69, v71, v69
	v_add_f32_e32 v71, v69, v73
	v_add_f32_e32 v66, 1.0, v66
	v_add_f32_e32 v67, 1.0, v67
	v_rcp_f32_e32 v66, v66
	v_rcp_f32_e32 v67, v67
	ds_write2_b32 v72, v69, v71 offset0:72 offset1:140
	v_sub_f32_e32 v69, 1.0, v70
	v_fma_f32 v72, v178, v66, v1
	v_fma_f32 v76, v178, v67, v1
	v_mov_b32_e32 v66, v218
	v_mov_b32_e32 v67, v219
	v_log_f32_e32 v73, v72
	v_log_f32_e32 v77, v76
	v_add_u32_e32 v70, 0x3400, v179
	ds_write2_b32 v70, v68, v69 offset0:72 offset1:140
	v_mul_f32_e32 v66, 0xbfb8aa3b, v66
	v_exp_f32_e32 v66, v66
	v_mul_f32_e32 v67, 0xbfb8aa3b, v67
	v_exp_f32_e32 v67, v67
	v_add_f32_e32 v68, v71, v73
	v_add_f32_e32 v66, 1.0, v66
	v_rcp_f32_e32 v66, v66
	v_add_f32_e32 v70, v68, v77
	v_sub_f32_e32 v69, 1.0, v72
	ds_write2_b32 v75, v68, v70 offset0:80 offset1:148
	v_sub_f32_e32 v68, 1.0, v76
	v_add_u32_e32 v71, 0x3600, v179
	ds_write2_b32 v71, v69, v68 offset0:80 offset1:148
	v_fma_f32 v68, v178, v66, v1
	v_add_f32_e32 v66, 1.0, v67
	v_add_u32_e32 v72, 0x1800, v179
	v_rcp_f32_e32 v71, v66
	v_mov_b32_e32 v66, v220
	v_mov_b32_e32 v67, v221
	v_log_f32_e32 v69, v68
	v_add_u32_e32 v77, 0x1a00, v179
	v_sub_f32_e32 v68, 1.0, v68
	v_mul_f32_e32 v66, 0xbfb8aa3b, v66
	v_exp_f32_e32 v66, v66
	v_mul_f32_e32 v67, 0xbfb8aa3b, v67
	v_exp_f32_e32 v67, v67
	v_add_f32_e32 v69, v70, v69
	v_add_f32_e32 v66, 1.0, v66
	v_rcp_f32_e32 v66, v66
	v_fma_f32 v70, v178, v71, v1
	v_log_f32_e32 v71, v70
	v_fma_f32 v73, v178, v66, v1
	v_add_f32_e32 v66, 1.0, v67
	v_rcp_f32_e32 v76, v66
	v_mov_b32_e32 v66, v222
	v_mov_b32_e32 v67, v223
	v_add_f32_e32 v71, v69, v71
	ds_write2_b32 v78, v69, v71 offset0:88 offset1:156
	v_sub_f32_e32 v69, 1.0, v70
	v_add_u32_e32 v70, 0x3800, v179
	v_mul_f32_e32 v66, 0xbfb8aa3b, v66
	v_exp_f32_e32 v66, v66
	v_log_f32_e32 v75, v73
	ds_write2_b32 v70, v68, v69 offset0:88 offset1:156
	v_fma_f32 v69, v178, v76, v1
	v_log_f32_e32 v70, v69
	v_add_f32_e32 v66, 1.0, v66
	v_mul_f32_e32 v67, 0xbfb8aa3b, v67
	v_rcp_f32_e32 v66, v66
	v_exp_f32_e32 v67, v67
	v_add_f32_e32 v68, v71, v75
	v_add_f32_e32 v70, v68, v70
	ds_write2_b32 v72, v68, v70 offset0:96 offset1:164
	v_sub_f32_e32 v68, 1.0, v69
	v_fma_f32 v69, v178, v66, v1
	v_add_f32_e32 v67, 1.0, v67
	v_log_f32_e32 v66, v69
	v_rcp_f32_e32 v67, v67
	v_sub_f32_e32 v71, 1.0, v73
	v_add_u32_e32 v72, 0x3a00, v179
	ds_write2_b32 v72, v71, v68 offset0:96 offset1:164
	v_add_u32_e32 v72, 0x1c00, v179
	v_add_f32_e32 v68, v70, v66
	v_fma_f32 v70, v178, v67, v1
	v_mov_b32_e32 v66, v234
	v_mov_b32_e32 v67, v235
	v_log_f32_e32 v71, v70
	v_sub_f32_e32 v69, 1.0, v69
	v_add_u32_e32 v75, 0x1e00, v179
	v_mov_b32_e32 v76, v74
	v_mul_f32_e32 v66, 0xbfb8aa3b, v66
	v_mul_f32_e32 v67, 0xbfb8aa3b, v67
	v_exp_f32_e32 v66, v66
	v_exp_f32_e32 v67, v67
	v_add_f32_e32 v71, v68, v71
	ds_write2_b32 v77, v68, v71 offset0:104 offset1:172
	v_add_f32_e32 v66, 1.0, v66
	v_add_f32_e32 v67, 1.0, v67
	v_rcp_f32_e32 v66, v66
	v_rcp_f32_e32 v67, v67
	v_sub_f32_e32 v68, 1.0, v70
	v_add_u32_e32 v70, 0x3c00, v179
	ds_write2_b32 v70, v69, v68 offset0:104 offset1:172
	v_fma_f32 v68, v178, v66, v1
	v_fma_f32 v70, v178, v67, v1
	v_mov_b32_e32 v66, v236
	v_mov_b32_e32 v67, v237
	v_log_f32_e32 v69, v68
	v_log_f32_e32 v73, v70
	v_sub_f32_e32 v68, 1.0, v68
	v_mov_b32_e32 v77, v74
	v_mul_f32_e32 v66, 0xbfb8aa3b, v66
	v_exp_f32_e32 v66, v66
	v_mul_f32_e32 v67, 0xbfb8aa3b, v67
	v_exp_f32_e32 v67, v67
	v_add_f32_e32 v69, v71, v69
	v_add_f32_e32 v66, 1.0, v66
	v_rcp_f32_e32 v66, v66
	v_add_f32_e32 v67, 1.0, v67
	v_rcp_f32_e32 v67, v67
	v_add_f32_e32 v71, v69, v73
	v_fma_f32 v66, v178, v66, v1
	ds_write2_b32 v72, v69, v71 offset0:112 offset1:180
	v_log_f32_e32 v72, v66
	v_fma_f32 v67, v178, v67, v1
	v_log_f32_e32 v73, v67
	v_sub_f32_e32 v69, 1.0, v70
	v_add_u32_e32 v70, 0x3e00, v179
	ds_write2_b32 v70, v68, v69 offset0:112 offset1:180
	v_add_f32_e32 v68, v71, v72
	v_add_f32_e32 v69, v68, v73
	ds_write2_b32 v75, v68, v69 offset0:120 offset1:188
	v_exp_f32_e32 v68, v69
	v_sub_f32_e32 v66, 1.0, v66
	v_sub_f32_e32 v67, 1.0, v67
	v_add_u32_e32 v70, 0x4000, v179
	ds_write2_b32 v70, v66, v67 offset0:120 offset1:188
	ds_write2st64_b32 v179, v68, v69 offset0:122 offset1:123
	ds_read_b128 v[156:159], v184 offset:26112
	ds_read_b128 v[148:151], v184 offset:26144
	ds_read_b128 v[160:163], v184 offset:28672
	ds_read_b128 v[152:155], v184 offset:28704
	v_mov_b32_e32 v75, v74
	v_mov_b32_e32 v78, v74
